# v27 + LayerNorm-1 router-logit MFMA loops: eight activation loads per iteration issued together with counted waits
# baseline (speedup 1.0000x reference)
.LBB0_1214:
	v_lshl_add_u64 v[22:23], v[20:21], 0, s[0:1]
	v_add_co_u32_e32 v34, vcc, s8, v22
	s_add_u32 s0, s0, 0x100
	s_nop 0
	v_addc_co_u32_e32 v35, vcc, 0, v23, vcc
	global_load_dwordx4 v[160:163], v[34:35], off
	global_load_dwordx4 v[164:167], v[34:35], off offset:32
	global_load_dwordx4 v[168:171], v[34:35], off offset:64
	global_load_dwordx4 v[172:175], v[34:35], off offset:96
	global_load_dwordx4 v[176:179], v[34:35], off offset:128
	global_load_dwordx4 v[180:183], v[34:35], off offset:160
	global_load_dwordx4 v[184:187], v[34:35], off offset:192
	global_load_dwordx4 v[188:191], v[34:35], off offset:224
	ds_read_b128 v[26:29], v2 offset:33280
	ds_read_b128 v[30:33], v2
	ds_read_b128 v[54:57], v2 offset:32
	s_addc_u32 s1, s1, 0
	s_cmpk_eq_i32 s0, 0x400
	s_waitcnt vmcnt(7) lgkmcnt(1)
	v_mfma_f32_32x32x16_bf16 v[4:19], v[30:33], v[160:163], v[4:19]
	v_mfma_f32_32x32x16_bf16 v[4:19], v[26:29], v[160:163], v[4:19]
	ds_read_b128 v[26:29], v2 offset:33312
	s_waitcnt vmcnt(6) lgkmcnt(1)
	v_mfma_f32_32x32x16_bf16 v[4:19], v[54:57], v[164:167], v[4:19]
	s_waitcnt lgkmcnt(0)
	v_mfma_f32_32x32x16_bf16 v[4:19], v[26:29], v[164:167], v[4:19]
	ds_read_b128 v[26:29], v2 offset:64
	ds_read_b128 v[30:33], v2 offset:33344
	s_waitcnt vmcnt(5) lgkmcnt(1)
	v_mfma_f32_32x32x16_bf16 v[4:19], v[26:29], v[168:171], v[4:19]
	s_waitcnt lgkmcnt(0)
	v_mfma_f32_32x32x16_bf16 v[4:19], v[30:33], v[168:171], v[4:19]
	ds_read_b128 v[26:29], v2 offset:96
	ds_read_b128 v[30:33], v2 offset:33376
	s_waitcnt vmcnt(4) lgkmcnt(1)
	v_mfma_f32_32x32x16_bf16 v[4:19], v[26:29], v[172:175], v[4:19]
	s_waitcnt lgkmcnt(0)
	v_mfma_f32_32x32x16_bf16 v[4:19], v[30:33], v[172:175], v[4:19]
	ds_read_b128 v[26:29], v2 offset:128
	ds_read_b128 v[30:33], v2 offset:33408
	s_waitcnt vmcnt(3) lgkmcnt(1)
	v_mfma_f32_32x32x16_bf16 v[4:19], v[26:29], v[176:179], v[4:19]
	s_waitcnt lgkmcnt(0)
	v_mfma_f32_32x32x16_bf16 v[4:19], v[30:33], v[176:179], v[4:19]
	ds_read_b128 v[26:29], v2 offset:160
	ds_read_b128 v[30:33], v2 offset:33440
	s_waitcnt vmcnt(2) lgkmcnt(1)
	v_mfma_f32_32x32x16_bf16 v[4:19], v[26:29], v[180:183], v[4:19]
	s_waitcnt lgkmcnt(0)
	v_mfma_f32_32x32x16_bf16 v[4:19], v[30:33], v[180:183], v[4:19]
	ds_read_b128 v[26:29], v2 offset:192
	ds_read_b128 v[30:33], v2 offset:33472
	s_waitcnt vmcnt(1) lgkmcnt(1)
	v_mfma_f32_32x32x16_bf16 v[4:19], v[26:29], v[184:187], v[4:19]
	s_waitcnt lgkmcnt(0)
	v_mfma_f32_32x32x16_bf16 v[4:19], v[30:33], v[184:187], v[4:19]
	ds_read_b128 v[26:29], v2 offset:224
	ds_read_b128 v[30:33], v2 offset:33504
	v_add_u32_e32 v2, 0x100, v2
	s_waitcnt vmcnt(0) lgkmcnt(1)
	v_mfma_f32_32x32x16_bf16 v[4:19], v[26:29], v[188:191], v[4:19]
	s_waitcnt lgkmcnt(0)
	v_mfma_f32_32x32x16_bf16 v[4:19], v[30:33], v[188:191], v[4:19]
	s_cbranch_scc0 .LBB0_1214
	s_barrier
	s_and_saveexec_b64 s[0:1], s[6:7]
	s_movk_i32 s10, 0x800
	s_movk_i32 s11, 0xdff
	s_mov_b32 s12, 0x8200
	s_cbranch_execz .LBB0_1218
	s_mov_b64 s[8:9], 0
	v_mov_b32_e32 v22, v36

.LBB0_1219:
	v_lshl_add_u64 v[22:23], v[20:21], 0, s[0:1]
	v_add_co_u32_e32 v34, vcc, 0x2e00000, v22
	s_add_u32 s0, s0, 0x100
	s_nop 0
	v_addc_co_u32_e32 v35, vcc, 0, v23, vcc
	global_load_dwordx4 v[160:163], v[34:35], off offset:1024
	global_load_dwordx4 v[164:167], v[34:35], off offset:1056
	global_load_dwordx4 v[168:171], v[34:35], off offset:1088
	global_load_dwordx4 v[172:175], v[34:35], off offset:1120
	global_load_dwordx4 v[176:179], v[34:35], off offset:1152
	global_load_dwordx4 v[180:183], v[34:35], off offset:1184
	global_load_dwordx4 v[184:187], v[34:35], off offset:1216
	global_load_dwordx4 v[188:191], v[34:35], off offset:1248
	ds_read_b128 v[26:29], v2 offset:33280
	ds_read_b128 v[30:33], v2
	ds_read_b128 v[54:57], v2 offset:32
	s_addc_u32 s1, s1, 0
	s_cmpk_lg_i32 s0, 0x400
	s_waitcnt vmcnt(7) lgkmcnt(1)
	v_mfma_f32_32x32x16_bf16 v[4:19], v[30:33], v[160:163], v[4:19]
	v_mfma_f32_32x32x16_bf16 v[4:19], v[26:29], v[160:163], v[4:19]
	ds_read_b128 v[26:29], v2 offset:33312
	s_waitcnt vmcnt(6) lgkmcnt(1)
	v_mfma_f32_32x32x16_bf16 v[4:19], v[54:57], v[164:167], v[4:19]
	s_waitcnt lgkmcnt(0)
	v_mfma_f32_32x32x16_bf16 v[4:19], v[26:29], v[164:167], v[4:19]
	ds_read_b128 v[26:29], v2 offset:64
	ds_read_b128 v[30:33], v2 offset:33344
	s_waitcnt vmcnt(5) lgkmcnt(1)
	v_mfma_f32_32x32x16_bf16 v[4:19], v[26:29], v[168:171], v[4:19]
	s_waitcnt lgkmcnt(0)
	v_mfma_f32_32x32x16_bf16 v[4:19], v[30:33], v[168:171], v[4:19]
	ds_read_b128 v[26:29], v2 offset:96
	ds_read_b128 v[30:33], v2 offset:33376
	s_waitcnt vmcnt(4) lgkmcnt(1)
	v_mfma_f32_32x32x16_bf16 v[4:19], v[26:29], v[172:175], v[4:19]
	s_waitcnt lgkmcnt(0)
	v_mfma_f32_32x32x16_bf16 v[4:19], v[30:33], v[172:175], v[4:19]
	ds_read_b128 v[26:29], v2 offset:128
	ds_read_b128 v[30:33], v2 offset:33408
	s_waitcnt vmcnt(3) lgkmcnt(1)
	v_mfma_f32_32x32x16_bf16 v[4:19], v[26:29], v[176:179], v[4:19]
	s_waitcnt lgkmcnt(0)
	v_mfma_f32_32x32x16_bf16 v[4:19], v[30:33], v[176:179], v[4:19]
	ds_read_b128 v[26:29], v2 offset:160
	ds_read_b128 v[30:33], v2 offset:33440
	s_waitcnt vmcnt(2) lgkmcnt(1)
	v_mfma_f32_32x32x16_bf16 v[4:19], v[26:29], v[180:183], v[4:19]
	s_waitcnt lgkmcnt(0)
	v_mfma_f32_32x32x16_bf16 v[4:19], v[30:33], v[180:183], v[4:19]
	ds_read_b128 v[26:29], v2 offset:192
	ds_read_b128 v[30:33], v2 offset:33472
	s_waitcnt vmcnt(1) lgkmcnt(1)
	v_mfma_f32_32x32x16_bf16 v[4:19], v[26:29], v[184:187], v[4:19]
	s_waitcnt lgkmcnt(0)
	v_mfma_f32_32x32x16_bf16 v[4:19], v[30:33], v[184:187], v[4:19]
	ds_read_b128 v[26:29], v2 offset:224
	ds_read_b128 v[30:33], v2 offset:33504
	v_add_u32_e32 v2, 0x100, v2
	s_waitcnt vmcnt(0) lgkmcnt(1)
	v_mfma_f32_32x32x16_bf16 v[4:19], v[26:29], v[188:191], v[4:19]
	s_waitcnt lgkmcnt(0)
	v_mfma_f32_32x32x16_bf16 v[4:19], v[30:33], v[188:191], v[4:19]
	s_cbranch_scc1 .LBB0_1219
	global_load_dwordx4 v[30:33], v[48:49], off
	s_nop 9
	v_mul_f32_e32 v2, 0xbfb8aa3b, v4
	v_exp_f32_e32 v2, v2
	s_nop 0
	v_add_f32_e32 v2, 1.0, v2
	v_div_scale_f32 v4, s[0:1], v2, v2, 1.0
	v_rcp_f32_e32 v20, v4
	s_nop 0
	v_fma_f32 v21, -v4, v20, 1.0
	v_fmac_f32_e32 v20, v21, v20
	v_div_scale_f32 v21, vcc, 1.0, v2, 1.0
	v_mul_f32_e32 v22, v21, v20
	v_fma_f32 v23, -v4, v22, v21
	v_fmac_f32_e32 v22, v23, v20
	v_fma_f32 v4, -v4, v22, v21
	v_div_fmas_f32 v4, v4, v20, v22
	v_div_fixup_f32 v35, v4, v2, 1.0
	v_mul_f32_e32 v2, 0xbfb8aa3b, v5
	v_exp_f32_e32 v2, v2
	s_waitcnt vmcnt(0)
	v_add_f32_e32 v4, v35, v30
	v_add_f32_e32 v2, 1.0, v2
	v_div_scale_f32 v5, s[0:1], v2, v2, 1.0
	v_rcp_f32_e32 v20, v5
	s_mov_b32 s0, 0xf149f2ca
	v_max_f32_e32 v53, 0xf149f2ca, v4
	v_cmp_lt_f32_e64 s[10:11], s0, v4
	v_fma_f32 v21, -v5, v20, 1.0
	v_fmac_f32_e32 v20, v21, v20
	v_div_scale_f32 v21, vcc, 1.0, v2, 1.0
	v_mul_f32_e32 v22, v21, v20
	v_fma_f32 v23, -v5, v22, v21
	v_fmac_f32_e32 v22, v23, v20
	v_fma_f32 v5, -v5, v22, v21
	v_div_fmas_f32 v5, v5, v20, v22
	v_div_fixup_f32 v34, v5, v2, 1.0
	v_add_f32_e32 v2, v34, v31
	global_load_dwordx4 v[28:31], v[48:49], off offset:32
	global_load_dwordx4 v[24:27], v[48:49], off offset:64
	global_load_dwordx4 v[20:23], v[48:49], off offset:96
	v_cmp_ngt_f32_e64 s[8:9], v2, v53
	v_mov_b32_e32 v57, v2
	v_mov_b32_e32 v5, v53
	s_and_saveexec_b64 s[0:1], s[8:9]
	s_cbranch_execz .LBB0_1224
	v_mov_b32_e32 v5, 0xf149f2ca
	v_cmp_gt_f32_e32 vcc, v2, v5
	s_and_saveexec_b64 s[12:13], vcc
	v_mov_b32_e32 v5, v2
	s_or_b64 exec, exec, s[12:13]
	v_mov_b32_e32 v57, v53
